# router logit section: the 64 packed v_pk_add_f32 (hi/lo split) beside the MFMAs split into scalar v_sub_f32 pairs, on top of v024
# baseline (speedup 1.0000x reference)
; #define LAS __attribute__((address_space(3)))
; __device__ __forceinline__ unsigned cvt_pk_bf16(float lo, float hi) { const bf16x2_t r = __builtin_convertvector((f32x2_t){lo, hi}, bf16x2_t); return __builtin_bit_cast(unsigned, r); }
; template <int MODE>
; __device__ __forceinline__ void norm_phase(const MkArgs& a, LAS unsigned char* lds, const int l, const int wv) {
;     ...
;         float tot = 0.f;
; #pragma unroll
;         for (int i = 0; i < 8; ++i) tot += ssp[i * 16 + r];
;         const float rstd = 1.0f / sqrtf(tot * (1.0f / DM) + EPSV);
; #pragma unroll
;         for (int j = 0; j < 8; ++j) {
;             const int k = 256 * w + 32 * j + 8 * q;
;             const f32x4 g0 = *(const LAS f32x4*)&tabA[k], g1 = *(const LAS f32x4*)&tabA[k + 4];
;             float gg[8] = {g0[0], g0[1], g0[2], g0[3], g1[0], g1[1], g1[2], g1[3]};
;             if constexpr (MODE != 3) {
;                 const f32x4 s0 = *(const LAS f32x4*)&tabB[k], s1 = *(const LAS f32x4*)&tabB[k + 4];
;                 const float sv[8] = {s0[0], s0[1], s0[2], s0[3], s1[0], s1[1], s1[2], s1[3]};
; #pragma unroll
;                 for (int i = 0; i < 8; ++i) xv[8 * j + i] = (xv[8 * j + i] * rstd) * gg[i] + sv[i];
;                 u32x4 o; o[0] = cvt_pk_bf16(xv[8 * j + 0], xv[8 * j + 1]); o[1] = cvt_pk_bf16(xv[8 * j + 2], xv[8 * j + 3]);
;                 o[2] = cvt_pk_bf16(xv[8 * j + 4], xv[8 * j + 5]); o[3] = cvt_pk_bf16(xv[8 * j + 6], xv[8 * j + 7]);
;                 *(u32x4*)(hb + (size_t)t * DM + k) = o;
.LBB0_901:
	s_or_b64 exec, exec, s[12:13]
	s_waitcnt lgkmcnt(0)
	s_barrier
	ds_read2_b32 v[84:85], v151 offset1:16
	ds_read2_b32 v[86:87], v151 offset0:32 offset1:48
	ds_read2_b32 v[88:89], v151 offset0:64 offset1:80
	s_mov_b32 s12, 0xf800000
	v_lshlrev_b64 v[82:83], 12, v[82:83]
	s_waitcnt lgkmcnt(2)
	v_add_f32_e32 v76, 0, v84
	v_add_f32_e32 v76, v76, v85
	ds_read2_b32 v[84:85], v151 offset0:96 offset1:112
	s_waitcnt lgkmcnt(2)
	v_add_f32_e32 v76, v76, v86
	v_add_f32_e32 v76, v76, v87
	s_waitcnt lgkmcnt(1)
	v_add_f32_e32 v76, v76, v88
	v_add_f32_e32 v76, v76, v89
	s_waitcnt lgkmcnt(0)
	v_add_f32_e32 v76, v76, v84
	v_add_f32_e32 v76, v76, v85
	v_fmamk_f32 v76, v76, 0x3a000000, v154
	v_mul_f32_e32 v84, 0x4f800000, v76
	v_cmp_gt_f32_e32 vcc, s12, v76
	v_lshl_add_u64 v[172:173], v[70:71], 0, v[82:83]
	s_nop 0
	v_cndmask_b32_e32 v76, v76, v84, vcc
	v_sqrt_f32_e32 v84, v76
	s_nop 0
	v_add_u32_e32 v85, -1, v84
	v_fma_f32 v86, -v85, v84, v76
	v_cmp_ge_f32_e64 s[12:13], 0, v86
	v_add_u32_e32 v86, 1, v84
	s_nop 0
	v_cndmask_b32_e64 v85, v84, v85, s[12:13]
	v_fma_f32 v84, -v86, v84, v76
	v_cmp_lt_f32_e64 s[12:13], 0, v84
	s_nop 1
	v_cndmask_b32_e64 v84, v85, v86, s[12:13]
	v_mul_f32_e32 v85, 0x37800000, v84
	v_cndmask_b32_e32 v84, v84, v85, vcc
	v_cmp_class_f32_e32 vcc, v76, v155
	s_nop 1
	v_cndmask_b32_e32 v76, v84, v76, vcc
	v_div_scale_f32 v84, s[12:13], v76, v76, 1.0
	v_rcp_f32_e32 v85, v84
	s_movk_i32 s12, 0x2000
	v_fma_f32 v86, -v84, v85, 1.0
	v_fmac_f32_e32 v85, v86, v85
	v_div_scale_f32 v86, vcc, 1.0, v76, 1.0
	v_mul_f32_e32 v87, v86, v85
	v_fma_f32 v88, -v84, v87, v86
	v_fmac_f32_e32 v87, v88, v85
	v_fma_f32 v84, -v84, v87, v86
	v_div_fmas_f32 v84, v84, v85, v87
	v_div_fixup_f32 v76, v84, v76, 1.0
	ds_read_b128 v[84:87], v65
	ds_read_b128 v[88:91], v118
	ds_read_b128 v[92:95], v117
	ds_read_b128 v[96:99], v119
	v_pk_mul_f32 v[60:61], v[60:61], v[76:77] op_sel_hi:[1,0]
	v_pk_mul_f32 v[44:45], v[44:45], v[76:77] op_sel_hi:[1,0]
	v_pk_mul_f32 v[56:57], v[56:57], v[76:77] op_sel_hi:[1,0]
	s_waitcnt lgkmcnt(2)
	v_pk_fma_f32 v[108:109], v[84:85], v[60:61], v[88:89]
	v_pk_mul_f32 v[60:61], v[62:63], v[76:77] op_sel_hi:[1,0]
	s_waitcnt lgkmcnt(0)
	v_pk_fma_f32 v[106:107], v[92:93], v[44:45], v[96:97]
	v_pk_mul_f32 v[44:45], v[46:47], v[76:77] op_sel_hi:[1,0]
	v_pk_fma_f32 v[112:113], v[86:87], v[60:61], v[90:91]
	v_pk_fma_f32 v[110:111], v[94:95], v[44:45], v[98:99]
	v_cvt_pk_bf16_f32 v44, v108, v109
	v_cvt_pk_bf16_f32 v45, v112, v113
	v_cvt_pk_bf16_f32 v46, v106, v107
	v_cvt_pk_bf16_f32 v47, v110, v111
	ds_read_b128 v[60:63], v120
	ds_read_b128 v[82:85], v122
	global_store_dwordx4 v[172:173], v[44:47], off
	ds_read_b128 v[86:89], v121
	ds_read_b128 v[90:93], v123
	v_pk_mul_f32 v[24:25], v[24:25], v[76:77] op_sel_hi:[1,0]
	v_pk_mul_f32 v[52:53], v[52:53], v[76:77] op_sel_hi:[1,0]
	s_waitcnt lgkmcnt(2)
	v_pk_fma_f32 v[98:99], v[56:57], v[60:61], v[82:83]
	v_pk_mul_f32 v[56:57], v[58:59], v[76:77] op_sel_hi:[1,0]
	s_waitcnt lgkmcnt(0)
	v_pk_fma_f32 v[100:101], v[24:25], v[86:87], v[90:91]
	v_pk_mul_f32 v[24:25], v[26:27], v[76:77] op_sel_hi:[1,0]
	v_pk_fma_f32 v[102:103], v[56:57], v[62:63], v[84:85]
	v_pk_fma_f32 v[104:105], v[24:25], v[88:89], v[92:93]
	v_cvt_pk_bf16_f32 v24, v98, v99
	v_cvt_pk_bf16_f32 v25, v102, v103
	v_cvt_pk_bf16_f32 v26, v100, v101
	v_cvt_pk_bf16_f32 v27, v104, v105
	ds_read_b128 v[56:59], v124
	ds_read_b128 v[60:63], v126
	global_store_dwordx4 v[172:173], v[24:27], off offset:64
	ds_read_b128 v[82:85], v125
	ds_read_b128 v[86:89], v127
	v_pk_mul_f32 v[4:5], v[4:5], v[76:77] op_sel_hi:[1,0]
	v_pk_mul_f32 v[48:49], v[48:49], v[76:77] op_sel_hi:[1,0]
	s_waitcnt lgkmcnt(2)
	v_pk_fma_f32 v[90:91], v[52:53], v[56:57], v[60:61]
	v_pk_mul_f32 v[52:53], v[54:55], v[76:77] op_sel_hi:[1,0]
	s_waitcnt lgkmcnt(0)
	v_pk_fma_f32 v[92:93], v[4:5], v[82:83], v[86:87]
	v_pk_mul_f32 v[4:5], v[6:7], v[76:77] op_sel_hi:[1,0]
	v_pk_fma_f32 v[94:95], v[52:53], v[58:59], v[62:63]
	v_pk_fma_f32 v[96:97], v[4:5], v[84:85], v[88:89]
	v_cvt_pk_bf16_f32 v4, v90, v91
	v_cvt_pk_bf16_f32 v5, v94, v95
	v_cvt_pk_bf16_f32 v6, v92, v93
	v_cvt_pk_bf16_f32 v7, v96, v97
	ds_read_b128 v[52:55], v128
	ds_read_b128 v[56:59], v130
	global_store_dwordx4 v[172:173], v[4:7], off offset:128
	ds_read_b128 v[60:63], v129
	ds_read_b128 v[82:85], v131
	v_pk_mul_f32 v[50:51], v[50:51], v[76:77] op_sel_hi:[1,0]
	v_pk_mul_f32 v[8:9], v[8:9], v[76:77] op_sel_hi:[1,0]
	s_waitcnt lgkmcnt(2)
	v_pk_fma_f32 v[48:49], v[48:49], v[52:53], v[56:57]
	v_pk_fma_f32 v[52:53], v[50:51], v[54:55], v[58:59]
	s_waitcnt lgkmcnt(0)
	v_pk_fma_f32 v[50:51], v[8:9], v[60:61], v[82:83]
	v_pk_mul_f32 v[8:9], v[10:11], v[76:77] op_sel_hi:[1,0]
	v_cvt_pk_bf16_f32 v10, v50, v51
	v_pk_fma_f32 v[54:55], v[8:9], v[62:63], v[84:85]
	v_cvt_pk_bf16_f32 v8, v48, v49
	v_cvt_pk_bf16_f32 v9, v52, v53
	v_cvt_pk_bf16_f32 v11, v54, v55
	ds_read_b128 v[56:59], v132
	ds_read_b128 v[60:63], v134
	global_store_dwordx4 v[172:173], v[8:11], off offset:192
	ds_read_b128 v[82:85], v133
	ds_read_b128 v[86:89], v135
	v_pk_mul_f32 v[40:41], v[40:41], v[76:77] op_sel_hi:[1,0]
	v_pk_mul_f32 v[42:43], v[42:43], v[76:77] op_sel_hi:[1,0]
	v_pk_mul_f32 v[12:13], v[12:13], v[76:77] op_sel_hi:[1,0]
	s_waitcnt lgkmcnt(2)
	v_pk_fma_f32 v[40:41], v[40:41], v[56:57], v[60:61]
	v_pk_fma_f32 v[56:57], v[42:43], v[58:59], v[62:63]
	s_waitcnt lgkmcnt(0)
; #define RT_LOAD(fr, c) do { _Pragma("unroll") for (int i = 0; i < 16; ++i) fr[i] = WFRAG((c) * 16 + i); } while (0)
; template <int MODE>
; __device__ __forceinline__ void norm_phase(const MkArgs& a, LAS unsigned char* lds, const int l, const int wv) {
;     ...
;             u32x4 frA[16], frB[16];
;     ...
;             RT_LOAD(frA, 0); RT_LOAD(frB, 1);
;             RT_MMA(frA, 0);
;             RT_LOAD(frA, 2);
;             RT_MMA(frB, 1);
;             RT_MMA(frA, 2);
	v_pk_fma_f32 v[42:43], v[12:13], v[82:83], v[86:87]
	v_pk_mul_f32 v[12:13], v[14:15], v[76:77] op_sel_hi:[1,0]
	v_cvt_pk_bf16_f32 v14, v42, v43
	v_pk_fma_f32 v[58:59], v[12:13], v[84:85], v[88:89]
	v_cvt_pk_bf16_f32 v12, v40, v41
	v_cvt_pk_bf16_f32 v13, v56, v57
	v_cvt_pk_bf16_f32 v15, v58, v59
	ds_read_b128 v[60:63], v136
	ds_read_b128 v[82:85], v138
	global_store_dwordx4 v[172:173], v[12:15], off offset:256
	ds_read_b128 v[86:89], v137
	ds_read_b128 v[160:163], v139
	v_pk_mul_f32 v[36:37], v[36:37], v[76:77] op_sel_hi:[1,0]
	v_pk_mul_f32 v[38:39], v[38:39], v[76:77] op_sel_hi:[1,0]
	v_pk_mul_f32 v[16:17], v[16:17], v[76:77] op_sel_hi:[1,0]
	s_waitcnt lgkmcnt(2)
	v_pk_fma_f32 v[36:37], v[36:37], v[60:61], v[82:83]
	v_pk_fma_f32 v[60:61], v[38:39], v[62:63], v[84:85]
	s_waitcnt lgkmcnt(0)
	v_pk_fma_f32 v[38:39], v[16:17], v[86:87], v[160:161]
	v_pk_mul_f32 v[16:17], v[18:19], v[76:77] op_sel_hi:[1,0]
	v_cvt_pk_bf16_f32 v18, v38, v39
	v_pk_fma_f32 v[62:63], v[16:17], v[88:89], v[162:163]
	v_cvt_pk_bf16_f32 v16, v36, v37
	v_cvt_pk_bf16_f32 v17, v60, v61
	v_cvt_pk_bf16_f32 v19, v62, v63
	ds_read_b128 v[82:85], v140
	ds_read_b128 v[86:89], v142
	global_store_dwordx4 v[172:173], v[16:19], off offset:320
	ds_read_b128 v[160:163], v141
	ds_read_b128 v[164:167], v143
	v_pk_mul_f32 v[32:33], v[32:33], v[76:77] op_sel_hi:[1,0]
	v_pk_mul_f32 v[34:35], v[34:35], v[76:77] op_sel_hi:[1,0]
	v_pk_mul_f32 v[20:21], v[20:21], v[76:77] op_sel_hi:[1,0]
	s_waitcnt lgkmcnt(2)
	v_pk_fma_f32 v[32:33], v[32:33], v[82:83], v[86:87]
	v_pk_fma_f32 v[82:83], v[34:35], v[84:85], v[88:89]
	s_waitcnt lgkmcnt(0)
	v_pk_fma_f32 v[34:35], v[20:21], v[160:161], v[164:165]
	v_pk_mul_f32 v[20:21], v[22:23], v[76:77] op_sel_hi:[1,0]
	v_cvt_pk_bf16_f32 v22, v34, v35
	v_pk_fma_f32 v[84:85], v[20:21], v[162:163], v[166:167]
	v_cvt_pk_bf16_f32 v20, v32, v33
	v_cvt_pk_bf16_f32 v21, v82, v83
	v_cvt_pk_bf16_f32 v23, v84, v85
	ds_read_b128 v[86:89], v144
	ds_read_b128 v[160:163], v146
	global_store_dwordx4 v[172:173], v[20:23], off offset:384
	ds_read_b128 v[164:167], v145
	ds_read_b128 v[168:171], v147
	v_pk_mul_f32 v[28:29], v[28:29], v[76:77] op_sel_hi:[1,0]
	v_pk_mul_f32 v[30:31], v[30:31], v[76:77] op_sel_hi:[1,0]
	v_pk_mul_f32 v[0:1], v[0:1], v[76:77] op_sel_hi:[1,0]
	s_waitcnt lgkmcnt(2)
	v_pk_fma_f32 v[28:29], v[28:29], v[86:87], v[160:161]
	v_pk_fma_f32 v[86:87], v[30:31], v[88:89], v[162:163]
	s_waitcnt lgkmcnt(0)
	v_pk_fma_f32 v[30:31], v[0:1], v[164:165], v[168:169]
	v_pk_mul_f32 v[0:1], v[2:3], v[76:77] op_sel_hi:[1,0]
	v_cvt_pk_bf16_f32 v2, v30, v31
	v_pk_fma_f32 v[88:89], v[0:1], v[166:167], v[170:171]
	v_cvt_pk_bf16_f32 v0, v28, v29
	v_cvt_pk_bf16_f32 v1, v86, v87
	v_cvt_pk_bf16_f32 v3, v88, v89
	v_mov_b32_e32 v76, v152
	global_store_dwordx4 v[172:173], v[0:3], off offset:448
	global_load_dwordx4 v[160:163], v76, s[22:23]
	global_load_dwordx4 v[164:167], v76, s[22:23] offset:1024
	global_load_dwordx4 v[168:171], v76, s[22:23] offset:2048
	global_load_dwordx4 v[172:175], v76, s[22:23] offset:3072
	s_add_u32 s12, s22, 0x1000
	s_addc_u32 s13, s23, 0
	global_load_dwordx4 v[176:179], v76, s[12:13]
	global_load_dwordx4 v[180:183], v76, s[12:13] offset:1024
	global_load_dwordx4 v[184:187], v76, s[12:13] offset:2048
	global_load_dwordx4 v[188:191], v76, s[12:13] offset:3072
	s_add_u32 s12, s22, 0x2000
	s_addc_u32 s13, s23, 0
	global_load_dwordx4 v[192:195], v76, s[12:13]
	global_load_dwordx4 v[196:199], v76, s[12:13] offset:1024
	global_load_dwordx4 v[200:203], v76, s[12:13] offset:2048
	global_load_dwordx4 v[204:207], v76, s[12:13] offset:3072
	s_add_u32 s12, s22, 0x3000
	s_addc_u32 s13, s23, 0
	global_load_dwordx4 v[208:211], v76, s[12:13]
	global_load_dwordx4 v[212:215], v76, s[12:13] offset:1024
	global_load_dwordx4 v[216:219], v76, s[12:13] offset:2048
	global_load_dwordx4 v[220:223], v76, s[12:13] offset:3072
	s_add_u32 s12, s22, 0x4000
	s_addc_u32 s13, s23, 0
	global_load_dwordx4 v[224:227], v76, s[12:13]
	global_load_dwordx4 v[228:231], v76, s[12:13] offset:1024
	v_lshlrev_b32_e32 v248, 16, v44
	v_and_b32_e32 v249, 0xffff0000, v44
	v_sub_f32_e32 v108, v108, v248
	v_sub_f32_e32 v109, v109, v249
	v_cvt_pk_bf16_f32 v244, v108, v109
	v_lshlrev_b32_e32 v250, 16, v45
	v_and_b32_e32 v251, 0xffff0000, v45
	v_sub_f32_e32 v112, v112, v250
	v_sub_f32_e32 v113, v113, v251
	v_cvt_pk_bf16_f32 v245, v112, v113
	v_lshlrev_b32_e32 v248, 16, v46
	v_and_b32_e32 v249, 0xffff0000, v46
	v_sub_f32_e32 v106, v106, v248
	v_sub_f32_e32 v107, v107, v249
	v_cvt_pk_bf16_f32 v246, v106, v107
	v_lshlrev_b32_e32 v250, 16, v47
	v_and_b32_e32 v251, 0xffff0000, v47
	v_sub_f32_e32 v110, v110, v250
	v_sub_f32_e32 v111, v111, v251
	v_cvt_pk_bf16_f32 v247, v110, v111
	s_waitcnt vmcnt(12)
	v_mfma_f32_16x16x32_bf16 v[232:235], v[44:47], v[160:163], 0
	v_mfma_f32_16x16x32_bf16 v[236:239], v[44:47], v[168:171], 0
	v_mfma_f32_16x16x32_bf16 v[240:243], v[44:47], v[176:179], 0
	v_mfma_f32_16x16x32_bf16 v[232:235], v[44:47], v[164:167], v[232:235]
	v_mfma_f32_16x16x32_bf16 v[236:239], v[44:47], v[172:175], v[236:239]
	v_mfma_f32_16x16x32_bf16 v[240:243], v[44:47], v[180:183], v[240:243]
	v_mfma_f32_16x16x32_bf16 v[232:235], v[244:247], v[160:163], v[232:235]
	v_mfma_f32_16x16x32_bf16 v[236:239], v[244:247], v[168:171], v[236:239]
	v_mfma_f32_16x16x32_bf16 v[240:243], v[244:247], v[176:179], v[240:243]
	global_load_dwordx4 v[160:163], v76, s[12:13] offset:2048
	global_load_dwordx4 v[164:167], v76, s[12:13] offset:3072
	s_add_u32 s12, s22, 0x5000
	s_addc_u32 s13, s23, 0
	global_load_dwordx4 v[168:171], v76, s[12:13]
	global_load_dwordx4 v[172:175], v76, s[12:13] offset:1024
	global_load_dwordx4 v[176:179], v76, s[12:13] offset:2048
	global_load_dwordx4 v[180:183], v76, s[12:13] offset:3072
	v_lshlrev_b32_e32 v248, 16, v24
	v_and_b32_e32 v249, 0xffff0000, v24
	v_sub_f32_e32 v98, v98, v248
	v_sub_f32_e32 v99, v99, v249
	v_cvt_pk_bf16_f32 v244, v98, v99
	v_lshlrev_b32_e32 v250, 16, v25
	v_and_b32_e32 v251, 0xffff0000, v25
	v_sub_f32_e32 v102, v102, v250
	v_sub_f32_e32 v103, v103, v251
	v_cvt_pk_bf16_f32 v245, v102, v103
	v_lshlrev_b32_e32 v248, 16, v26
	v_and_b32_e32 v249, 0xffff0000, v26
	v_sub_f32_e32 v100, v100, v248
	v_sub_f32_e32 v101, v101, v249
	v_cvt_pk_bf16_f32 v246, v100, v101
	v_lshlrev_b32_e32 v250, 16, v27
	v_and_b32_e32 v251, 0xffff0000, v27
	v_sub_f32_e32 v104, v104, v250
	v_sub_f32_e32 v105, v105, v251
	v_cvt_pk_bf16_f32 v247, v104, v105
	s_waitcnt vmcnt(12)
; #define RT_LOAD(fr, c) do { _Pragma("unroll") for (int i = 0; i < 16; ++i) fr[i] = WFRAG((c) * 16 + i); } while (0)
; template <int MODE>
; __device__ __forceinline__ void norm_phase(const MkArgs& a, LAS unsigned char* lds, const int l, const int wv) {
;     ...
;             RT_LOAD(frA, 0); RT_LOAD(frB, 1);
;             RT_MMA(frA, 0);
;             RT_LOAD(frA, 2);
;             RT_MMA(frB, 1);
;             RT_MMA(frA, 2);
	v_mfma_f32_16x16x32_bf16 v[232:235], v[24:27], v[184:187], v[232:235]
	v_mfma_f32_16x16x32_bf16 v[236:239], v[24:27], v[192:195], v[236:239]
	v_mfma_f32_16x16x32_bf16 v[240:243], v[24:27], v[200:203], v[240:243]
	v_mfma_f32_16x16x32_bf16 v[232:235], v[24:27], v[188:191], v[232:235]
	v_mfma_f32_16x16x32_bf16 v[236:239], v[24:27], v[196:199], v[236:239]
	v_mfma_f32_16x16x32_bf16 v[240:243], v[24:27], v[204:207], v[240:243]
	v_mfma_f32_16x16x32_bf16 v[232:235], v[244:247], v[184:187], v[232:235]
	v_mfma_f32_16x16x32_bf16 v[236:239], v[244:247], v[192:195], v[236:239]
	v_mfma_f32_16x16x32_bf16 v[240:243], v[244:247], v[200:203], v[240:243]
	s_add_u32 s12, s22, 0x6000
	s_addc_u32 s13, s23, 0
	global_load_dwordx4 v[184:187], v76, s[12:13]
	global_load_dwordx4 v[188:191], v76, s[12:13] offset:1024
	global_load_dwordx4 v[192:195], v76, s[12:13] offset:2048
	global_load_dwordx4 v[196:199], v76, s[12:13] offset:3072
	s_add_u32 s12, s22, 0x7000
	s_addc_u32 s13, s23, 0
	global_load_dwordx4 v[200:203], v76, s[12:13]
	global_load_dwordx4 v[204:207], v76, s[12:13] offset:1024
	v_lshlrev_b32_e32 v248, 16, v4
	v_and_b32_e32 v249, 0xffff0000, v4
	v_sub_f32_e32 v90, v90, v248
	v_sub_f32_e32 v91, v91, v249
	v_cvt_pk_bf16_f32 v244, v90, v91
	v_lshlrev_b32_e32 v250, 16, v5
	v_and_b32_e32 v251, 0xffff0000, v5
	v_sub_f32_e32 v94, v94, v250
	v_sub_f32_e32 v95, v95, v251
	v_cvt_pk_bf16_f32 v245, v94, v95
	v_lshlrev_b32_e32 v248, 16, v6
	v_and_b32_e32 v249, 0xffff0000, v6
	v_sub_f32_e32 v92, v92, v248
	v_sub_f32_e32 v93, v93, v249
	v_cvt_pk_bf16_f32 v246, v92, v93
	v_lshlrev_b32_e32 v250, 16, v7
	v_and_b32_e32 v251, 0xffff0000, v7
	v_sub_f32_e32 v96, v96, v250
	v_sub_f32_e32 v97, v97, v251
	v_cvt_pk_bf16_f32 v247, v96, v97
	s_waitcnt vmcnt(12)
	v_mfma_f32_16x16x32_bf16 v[232:235], v[4:7], v[208:211], v[232:235]
	v_mfma_f32_16x16x32_bf16 v[236:239], v[4:7], v[216:219], v[236:239]
	v_mfma_f32_16x16x32_bf16 v[240:243], v[4:7], v[224:227], v[240:243]
	v_mfma_f32_16x16x32_bf16 v[232:235], v[4:7], v[212:215], v[232:235]
	v_mfma_f32_16x16x32_bf16 v[236:239], v[4:7], v[220:223], v[236:239]
	v_mfma_f32_16x16x32_bf16 v[240:243], v[4:7], v[228:231], v[240:243]
	v_mfma_f32_16x16x32_bf16 v[232:235], v[244:247], v[208:211], v[232:235]
	v_mfma_f32_16x16x32_bf16 v[236:239], v[244:247], v[216:219], v[236:239]
	v_mfma_f32_16x16x32_bf16 v[240:243], v[244:247], v[224:227], v[240:243]
	global_load_dwordx4 v[208:211], v76, s[12:13] offset:2048
	global_load_dwordx4 v[212:215], v76, s[12:13] offset:3072
	s_add_u32 s12, s22, 0x8000
	s_addc_u32 s13, s23, 0
	global_load_dwordx4 v[216:219], v76, s[12:13]
	global_load_dwordx4 v[220:223], v76, s[12:13] offset:1024
	global_load_dwordx4 v[224:227], v76, s[12:13] offset:2048
	global_load_dwordx4 v[228:231], v76, s[12:13] offset:3072
	v_lshlrev_b32_e32 v248, 16, v8
	v_and_b32_e32 v249, 0xffff0000, v8
	v_sub_f32_e32 v48, v48, v248
	v_sub_f32_e32 v49, v49, v249
	v_cvt_pk_bf16_f32 v244, v48, v49
	v_lshlrev_b32_e32 v250, 16, v9
	v_and_b32_e32 v251, 0xffff0000, v9
	v_sub_f32_e32 v52, v52, v250
	v_sub_f32_e32 v53, v53, v251
	v_cvt_pk_bf16_f32 v245, v52, v53
	v_lshlrev_b32_e32 v248, 16, v10
	v_and_b32_e32 v249, 0xffff0000, v10
	v_sub_f32_e32 v50, v50, v248
	v_sub_f32_e32 v51, v51, v249
	v_cvt_pk_bf16_f32 v246, v50, v51
	v_lshlrev_b32_e32 v250, 16, v11
	v_and_b32_e32 v251, 0xffff0000, v11
	v_sub_f32_e32 v54, v54, v250
	v_sub_f32_e32 v55, v55, v251
	v_cvt_pk_bf16_f32 v247, v54, v55
	s_waitcnt vmcnt(12)
	v_mfma_f32_16x16x32_bf16 v[232:235], v[8:11], v[160:163], v[232:235]
	v_mfma_f32_16x16x32_bf16 v[236:239], v[8:11], v[168:171], v[236:239]
	v_mfma_f32_16x16x32_bf16 v[240:243], v[8:11], v[176:179], v[240:243]
	v_mfma_f32_16x16x32_bf16 v[232:235], v[8:11], v[164:167], v[232:235]
	v_mfma_f32_16x16x32_bf16 v[236:239], v[8:11], v[172:175], v[236:239]
	v_mfma_f32_16x16x32_bf16 v[240:243], v[8:11], v[180:183], v[240:243]
	v_mfma_f32_16x16x32_bf16 v[232:235], v[244:247], v[160:163], v[232:235]
	v_mfma_f32_16x16x32_bf16 v[236:239], v[244:247], v[168:171], v[236:239]
	v_mfma_f32_16x16x32_bf16 v[240:243], v[244:247], v[176:179], v[240:243]
	s_add_u32 s12, s22, 0x9000
	s_addc_u32 s13, s23, 0
	global_load_dwordx4 v[160:163], v76, s[12:13]
	global_load_dwordx4 v[164:167], v76, s[12:13] offset:1024
	global_load_dwordx4 v[168:171], v76, s[12:13] offset:2048
	global_load_dwordx4 v[172:175], v76, s[12:13] offset:3072
	s_add_u32 s12, s22, 0xa000
	s_addc_u32 s13, s23, 0
	global_load_dwordx4 v[176:179], v76, s[12:13]
	global_load_dwordx4 v[180:183], v76, s[12:13] offset:1024
	v_lshlrev_b32_e32 v248, 16, v12
	v_and_b32_e32 v249, 0xffff0000, v12
	v_sub_f32_e32 v40, v40, v248
	v_sub_f32_e32 v41, v41, v249
	v_cvt_pk_bf16_f32 v244, v40, v41
	v_lshlrev_b32_e32 v250, 16, v13
	v_and_b32_e32 v251, 0xffff0000, v13
	v_sub_f32_e32 v56, v56, v250
	v_sub_f32_e32 v57, v57, v251
	v_cvt_pk_bf16_f32 v245, v56, v57
	v_lshlrev_b32_e32 v248, 16, v14
	v_and_b32_e32 v249, 0xffff0000, v14
	v_sub_f32_e32 v42, v42, v248
	v_sub_f32_e32 v43, v43, v249
	v_cvt_pk_bf16_f32 v246, v42, v43
	v_lshlrev_b32_e32 v250, 16, v15
	v_and_b32_e32 v251, 0xffff0000, v15
	v_sub_f32_e32 v58, v58, v250
	v_sub_f32_e32 v59, v59, v251
	v_cvt_pk_bf16_f32 v247, v58, v59
	s_waitcnt vmcnt(12)
; #define RT_LOAD(fr, c) do { _Pragma("unroll") for (int i = 0; i < 16; ++i) fr[i] = WFRAG((c) * 16 + i); } while (0)
; template <int MODE>
; __device__ __forceinline__ void norm_phase(const MkArgs& a, LAS unsigned char* lds, const int l, const int wv) {
;     ...
;             RT_LOAD(frA, 0); RT_LOAD(frB, 1);
;             RT_MMA(frA, 0);
;             RT_LOAD(frA, 2);
;             RT_MMA(frB, 1);
;             RT_MMA(frA, 2);
;     ...
; #pragma unroll
;             for (int nt = 0; nt < 3; ++nt)
; #pragma unroll
;                 for (int e = 0; e < 4; ++e) part[(w * 16 + 4 * q + e) * 48 + 16 * nt + r] = acc[nt][e];
;     ...
;             __syncthreads();
;             for (int o = tid; o < 16 * 36; o += 512) {
	v_mfma_f32_16x16x32_bf16 v[232:235], v[12:15], v[184:187], v[232:235]
	v_mfma_f32_16x16x32_bf16 v[236:239], v[12:15], v[192:195], v[236:239]
	v_mfma_f32_16x16x32_bf16 v[240:243], v[12:15], v[200:203], v[240:243]
	v_mfma_f32_16x16x32_bf16 v[232:235], v[12:15], v[188:191], v[232:235]
	v_mfma_f32_16x16x32_bf16 v[236:239], v[12:15], v[196:199], v[236:239]
	v_mfma_f32_16x16x32_bf16 v[240:243], v[12:15], v[204:207], v[240:243]
	v_mfma_f32_16x16x32_bf16 v[232:235], v[244:247], v[184:187], v[232:235]
	v_mfma_f32_16x16x32_bf16 v[236:239], v[244:247], v[192:195], v[236:239]
	v_mfma_f32_16x16x32_bf16 v[240:243], v[244:247], v[200:203], v[240:243]
	global_load_dwordx4 v[184:187], v76, s[12:13] offset:2048
	global_load_dwordx4 v[188:191], v76, s[12:13] offset:3072
	s_add_u32 s12, s22, 0xb000
	s_addc_u32 s13, s23, 0
	global_load_dwordx4 v[192:195], v76, s[12:13]
	global_load_dwordx4 v[196:199], v76, s[12:13] offset:1024
	global_load_dwordx4 v[200:203], v76, s[12:13] offset:2048
	global_load_dwordx4 v[204:207], v76, s[12:13] offset:3072
	v_lshlrev_b32_e32 v248, 16, v16
	v_and_b32_e32 v249, 0xffff0000, v16
	v_sub_f32_e32 v36, v36, v248
	v_sub_f32_e32 v37, v37, v249
	v_cvt_pk_bf16_f32 v244, v36, v37
	v_lshlrev_b32_e32 v250, 16, v17
	v_and_b32_e32 v251, 0xffff0000, v17
	v_sub_f32_e32 v60, v60, v250
	v_sub_f32_e32 v61, v61, v251
	v_cvt_pk_bf16_f32 v245, v60, v61
	v_lshlrev_b32_e32 v248, 16, v18
	v_and_b32_e32 v249, 0xffff0000, v18
	v_sub_f32_e32 v38, v38, v248
	v_sub_f32_e32 v39, v39, v249
	v_cvt_pk_bf16_f32 v246, v38, v39
	v_lshlrev_b32_e32 v250, 16, v19
	v_and_b32_e32 v251, 0xffff0000, v19
	v_sub_f32_e32 v62, v62, v250
	v_sub_f32_e32 v63, v63, v251
	v_cvt_pk_bf16_f32 v247, v62, v63
	s_waitcnt vmcnt(12)
	v_mfma_f32_16x16x32_bf16 v[232:235], v[16:19], v[208:211], v[232:235]
	v_mfma_f32_16x16x32_bf16 v[236:239], v[16:19], v[216:219], v[236:239]
	v_mfma_f32_16x16x32_bf16 v[240:243], v[16:19], v[224:227], v[240:243]
	v_mfma_f32_16x16x32_bf16 v[232:235], v[16:19], v[212:215], v[232:235]
	v_mfma_f32_16x16x32_bf16 v[236:239], v[16:19], v[220:223], v[236:239]
	v_mfma_f32_16x16x32_bf16 v[240:243], v[16:19], v[228:231], v[240:243]
	v_mfma_f32_16x16x32_bf16 v[232:235], v[244:247], v[208:211], v[232:235]
	v_mfma_f32_16x16x32_bf16 v[236:239], v[244:247], v[216:219], v[236:239]
	v_mfma_f32_16x16x32_bf16 v[240:243], v[244:247], v[224:227], v[240:243]
	v_lshlrev_b32_e32 v248, 16, v20
	v_and_b32_e32 v249, 0xffff0000, v20
	v_sub_f32_e32 v32, v32, v248
	v_sub_f32_e32 v33, v33, v249
	v_cvt_pk_bf16_f32 v244, v32, v33
	v_lshlrev_b32_e32 v250, 16, v21
	v_and_b32_e32 v251, 0xffff0000, v21
	v_sub_f32_e32 v82, v82, v250
	v_sub_f32_e32 v83, v83, v251
	v_cvt_pk_bf16_f32 v245, v82, v83
	v_lshlrev_b32_e32 v248, 16, v22
	v_and_b32_e32 v249, 0xffff0000, v22
	v_sub_f32_e32 v34, v34, v248
	v_sub_f32_e32 v35, v35, v249
	v_cvt_pk_bf16_f32 v246, v34, v35
	v_lshlrev_b32_e32 v250, 16, v23
	v_and_b32_e32 v251, 0xffff0000, v23
	v_sub_f32_e32 v84, v84, v250
	v_sub_f32_e32 v85, v85, v251
	v_cvt_pk_bf16_f32 v247, v84, v85
	s_waitcnt vmcnt(6)
	v_mfma_f32_16x16x32_bf16 v[232:235], v[20:23], v[160:163], v[232:235]
	v_mfma_f32_16x16x32_bf16 v[236:239], v[20:23], v[168:171], v[236:239]
	v_mfma_f32_16x16x32_bf16 v[240:243], v[20:23], v[176:179], v[240:243]
	v_mfma_f32_16x16x32_bf16 v[232:235], v[20:23], v[164:167], v[232:235]
	v_mfma_f32_16x16x32_bf16 v[236:239], v[20:23], v[172:175], v[236:239]
	v_mfma_f32_16x16x32_bf16 v[240:243], v[20:23], v[180:183], v[240:243]
	v_mfma_f32_16x16x32_bf16 v[232:235], v[244:247], v[160:163], v[232:235]
	v_mfma_f32_16x16x32_bf16 v[236:239], v[244:247], v[168:171], v[236:239]
	v_mfma_f32_16x16x32_bf16 v[240:243], v[244:247], v[176:179], v[240:243]
	v_lshlrev_b32_e32 v248, 16, v0
	v_and_b32_e32 v249, 0xffff0000, v0
	v_sub_f32_e32 v28, v28, v248
	v_sub_f32_e32 v29, v29, v249
	v_cvt_pk_bf16_f32 v244, v28, v29
	v_lshlrev_b32_e32 v250, 16, v1
	v_and_b32_e32 v251, 0xffff0000, v1
	v_sub_f32_e32 v86, v86, v250
	v_sub_f32_e32 v87, v87, v251
	v_cvt_pk_bf16_f32 v245, v86, v87
	v_lshlrev_b32_e32 v248, 16, v2
	v_and_b32_e32 v249, 0xffff0000, v2
	v_sub_f32_e32 v30, v30, v248
	v_sub_f32_e32 v31, v31, v249
	v_cvt_pk_bf16_f32 v246, v30, v31
	v_lshlrev_b32_e32 v250, 16, v3
	v_and_b32_e32 v251, 0xffff0000, v3
	v_sub_f32_e32 v88, v88, v250
	v_sub_f32_e32 v89, v89, v251
	v_cvt_pk_bf16_f32 v247, v88, v89
	s_waitcnt vmcnt(0)
	v_mfma_f32_16x16x32_bf16 v[232:235], v[0:3], v[184:187], v[232:235]
	v_mfma_f32_16x16x32_bf16 v[236:239], v[0:3], v[192:195], v[236:239]
	v_mfma_f32_16x16x32_bf16 v[240:243], v[0:3], v[200:203], v[240:243]
	v_mfma_f32_16x16x32_bf16 v[232:235], v[0:3], v[188:191], v[232:235]
	v_mfma_f32_16x16x32_bf16 v[236:239], v[0:3], v[196:199], v[236:239]
	v_mfma_f32_16x16x32_bf16 v[240:243], v[0:3], v[204:207], v[240:243]
	v_mfma_f32_16x16x32_bf16 v[232:235], v[244:247], v[184:187], v[232:235]
	v_mfma_f32_16x16x32_bf16 v[236:239], v[244:247], v[192:195], v[236:239]
	v_mfma_f32_16x16x32_bf16 v[240:243], v[244:247], v[200:203], v[240:243]
	v_add_u32_e32 v4, 0x400, v156
	s_nop 7
	s_nop 1
	ds_write2_b32 v4, v232, v236 offset1:16
	ds_write2_b32 v4, v234, v238 offset0:96 offset1:112
	ds_write2_b32 v4, v240, v233 offset0:32 offset1:48
	ds_write2_b32 v4, v237, v241 offset0:64 offset1:80
	ds_write2_b32 v4, v242, v235 offset0:128 offset1:144
	ds_write2_b32 v4, v239, v243 offset0:160 offset1:176
	s_waitcnt lgkmcnt(0)
	s_barrier
	s_and_saveexec_b64 s[12:13], s[4:5]
	s_cbranch_execz .LBB0_904
	s_mov_b64 s[14:15], 0
	v_mov_b32_e32 v0, v114
	v_mov_b32_e32 v2, v64

; #define LAS __attribute__((address_space(3)))
; __device__ __forceinline__ unsigned cvt_pk_bf16(float lo, float hi) { const bf16x2_t r = __builtin_convertvector((f32x2_t){lo, hi}, bf16x2_t); return __builtin_bit_cast(unsigned, r); }
; template <int MODE>
; __device__ __forceinline__ void norm_phase(const MkArgs& a, LAS unsigned char* lds, const int l, const int wv) {
;     ...
;         float tot = 0.f;
; #pragma unroll
;         for (int i = 0; i < 8; ++i) tot += ssp[i * 16 + r];
;         const float rstd = 1.0f / sqrtf(tot * (1.0f / DM) + EPSV);
; #pragma unroll
;         for (int j = 0; j < 8; ++j) {
;             const int k = 256 * w + 32 * j + 8 * q;
;             const f32x4 g0 = *(const LAS f32x4*)&tabA[k], g1 = *(const LAS f32x4*)&tabA[k + 4];
;             float gg[8] = {g0[0], g0[1], g0[2], g0[3], g1[0], g1[1], g1[2], g1[3]};
;             if constexpr (MODE != 3) {
;                 const f32x4 s0 = *(const LAS f32x4*)&tabB[k], s1 = *(const LAS f32x4*)&tabB[k + 4];
;                 const float sv[8] = {s0[0], s0[1], s0[2], s0[3], s1[0], s1[1], s1[2], s1[3]};
; #pragma unroll
;                 for (int i = 0; i < 8; ++i) xv[8 * j + i] = (xv[8 * j + i] * rstd) * gg[i] + sv[i];
;                 u32x4 o; o[0] = cvt_pk_bf16(xv[8 * j + 0], xv[8 * j + 1]); o[1] = cvt_pk_bf16(xv[8 * j + 2], xv[8 * j + 3]);
;                 o[2] = cvt_pk_bf16(xv[8 * j + 4], xv[8 * j + 5]); o[3] = cvt_pk_bf16(xv[8 * j + 6], xv[8 * j + 7]);
;                 *(u32x4*)(hb + (size_t)t * DM + k) = o;
.LBB0_1973:
	s_or_b64 exec, exec, s[12:13]
	s_waitcnt lgkmcnt(0)
	s_barrier
	ds_read2_b32 v[84:85], v118 offset1:16
	ds_read2_b32 v[86:87], v118 offset0:32 offset1:48
	ds_read2_b32 v[88:89], v118 offset0:64 offset1:80
	s_mov_b32 s12, 0xf800000
	v_lshlrev_b64 v[82:83], 12, v[82:83]
	s_waitcnt lgkmcnt(2)
	v_add_f32_e32 v76, 0, v84
	v_add_f32_e32 v76, v76, v85
	ds_read2_b32 v[84:85], v118 offset0:96 offset1:112
	s_waitcnt lgkmcnt(2)
	v_add_f32_e32 v76, v76, v86
	v_add_f32_e32 v76, v76, v87
	s_waitcnt lgkmcnt(1)
	v_add_f32_e32 v76, v76, v88
	v_add_f32_e32 v76, v76, v89
	s_waitcnt lgkmcnt(0)
	v_add_f32_e32 v76, v76, v84
	v_add_f32_e32 v76, v76, v85
	v_fmamk_f32 v76, v76, 0x3a000000, v154
	v_mul_f32_e32 v84, 0x4f800000, v76
	v_cmp_gt_f32_e32 vcc, s12, v76
	v_lshl_add_u64 v[172:173], v[74:75], 0, v[82:83]
	s_nop 0
	v_cndmask_b32_e32 v76, v76, v84, vcc
	v_sqrt_f32_e32 v84, v76
	s_nop 0
	v_add_u32_e32 v85, -1, v84
	v_fma_f32 v86, -v85, v84, v76
	v_cmp_ge_f32_e64 s[12:13], 0, v86
	v_add_u32_e32 v86, 1, v84
	s_nop 0
	v_cndmask_b32_e64 v85, v84, v85, s[12:13]
	v_fma_f32 v84, -v86, v84, v76
	v_cmp_lt_f32_e64 s[12:13], 0, v84
	s_nop 1
	v_cndmask_b32_e64 v84, v85, v86, s[12:13]
	v_mul_f32_e32 v85, 0x37800000, v84
	v_cndmask_b32_e32 v84, v84, v85, vcc
	v_cmp_class_f32_e32 vcc, v76, v155
	s_nop 1
	v_cndmask_b32_e32 v76, v84, v76, vcc
	v_div_scale_f32 v84, s[12:13], v76, v76, 1.0
	v_rcp_f32_e32 v85, v84
	s_movk_i32 s12, 0x2000
	v_fma_f32 v86, -v84, v85, 1.0
	v_fmac_f32_e32 v85, v86, v85
	v_div_scale_f32 v86, vcc, 1.0, v76, 1.0
	v_mul_f32_e32 v87, v86, v85
	v_fma_f32 v88, -v84, v87, v86
	v_fmac_f32_e32 v87, v88, v85
	v_fma_f32 v84, -v84, v87, v86
	v_div_fmas_f32 v84, v84, v85, v87
	v_div_fixup_f32 v76, v84, v76, 1.0
	ds_read_b128 v[84:87], v65
	ds_read_b128 v[88:91], v124
	ds_read_b128 v[92:95], v123
	ds_read_b128 v[96:99], v125
	v_pk_mul_f32 v[60:61], v[60:61], v[76:77] op_sel_hi:[1,0]
	v_pk_mul_f32 v[44:45], v[44:45], v[76:77] op_sel_hi:[1,0]
	v_pk_mul_f32 v[56:57], v[56:57], v[76:77] op_sel_hi:[1,0]
	s_waitcnt lgkmcnt(2)
	v_pk_fma_f32 v[108:109], v[84:85], v[60:61], v[88:89]
	v_pk_mul_f32 v[60:61], v[62:63], v[76:77] op_sel_hi:[1,0]
	s_waitcnt lgkmcnt(0)
	v_pk_fma_f32 v[106:107], v[92:93], v[44:45], v[96:97]
	v_pk_mul_f32 v[44:45], v[46:47], v[76:77] op_sel_hi:[1,0]
	v_pk_fma_f32 v[112:113], v[86:87], v[60:61], v[90:91]
	v_pk_fma_f32 v[110:111], v[94:95], v[44:45], v[98:99]
	v_cvt_pk_bf16_f32 v44, v108, v109
	v_cvt_pk_bf16_f32 v45, v112, v113
	v_cvt_pk_bf16_f32 v46, v106, v107
	v_cvt_pk_bf16_f32 v47, v110, v111
	ds_read_b128 v[60:63], v126
	ds_read_b128 v[82:85], v128
	global_store_dwordx4 v[172:173], v[44:47], off
	ds_read_b128 v[86:89], v127
	ds_read_b128 v[90:93], v129
	v_pk_mul_f32 v[24:25], v[24:25], v[76:77] op_sel_hi:[1,0]
	v_pk_mul_f32 v[52:53], v[52:53], v[76:77] op_sel_hi:[1,0]
	s_waitcnt lgkmcnt(2)
	v_pk_fma_f32 v[98:99], v[56:57], v[60:61], v[82:83]
	v_pk_mul_f32 v[56:57], v[58:59], v[76:77] op_sel_hi:[1,0]
	s_waitcnt lgkmcnt(0)
	v_pk_fma_f32 v[100:101], v[24:25], v[86:87], v[90:91]
	v_pk_mul_f32 v[24:25], v[26:27], v[76:77] op_sel_hi:[1,0]
	v_pk_fma_f32 v[102:103], v[56:57], v[62:63], v[84:85]
	v_pk_fma_f32 v[104:105], v[24:25], v[88:89], v[92:93]
	v_cvt_pk_bf16_f32 v24, v98, v99
	v_cvt_pk_bf16_f32 v25, v102, v103
	v_cvt_pk_bf16_f32 v26, v100, v101
	v_cvt_pk_bf16_f32 v27, v104, v105
	ds_read_b128 v[56:59], v130
	ds_read_b128 v[60:63], v132
	global_store_dwordx4 v[172:173], v[24:27], off offset:64
	ds_read_b128 v[82:85], v131
	ds_read_b128 v[86:89], v133
	v_pk_mul_f32 v[4:5], v[4:5], v[76:77] op_sel_hi:[1,0]
	v_pk_mul_f32 v[48:49], v[48:49], v[76:77] op_sel_hi:[1,0]
	s_waitcnt lgkmcnt(2)
	v_pk_fma_f32 v[90:91], v[52:53], v[56:57], v[60:61]
	v_pk_mul_f32 v[52:53], v[54:55], v[76:77] op_sel_hi:[1,0]
	s_waitcnt lgkmcnt(0)
	v_pk_fma_f32 v[92:93], v[4:5], v[82:83], v[86:87]
	v_pk_mul_f32 v[4:5], v[6:7], v[76:77] op_sel_hi:[1,0]
	v_pk_fma_f32 v[94:95], v[52:53], v[58:59], v[62:63]
	v_pk_fma_f32 v[96:97], v[4:5], v[84:85], v[88:89]
	v_cvt_pk_bf16_f32 v4, v90, v91
	v_cvt_pk_bf16_f32 v5, v94, v95
	v_cvt_pk_bf16_f32 v6, v92, v93
	v_cvt_pk_bf16_f32 v7, v96, v97
	ds_read_b128 v[52:55], v134
	ds_read_b128 v[56:59], v136
	global_store_dwordx4 v[172:173], v[4:7], off offset:128
	ds_read_b128 v[60:63], v135
	ds_read_b128 v[82:85], v137
	v_pk_mul_f32 v[50:51], v[50:51], v[76:77] op_sel_hi:[1,0]
	v_pk_mul_f32 v[8:9], v[8:9], v[76:77] op_sel_hi:[1,0]
	s_waitcnt lgkmcnt(2)
	v_pk_fma_f32 v[48:49], v[48:49], v[52:53], v[56:57]
	v_pk_fma_f32 v[52:53], v[50:51], v[54:55], v[58:59]
	s_waitcnt lgkmcnt(0)
	v_pk_fma_f32 v[50:51], v[8:9], v[60:61], v[82:83]
	v_pk_mul_f32 v[8:9], v[10:11], v[76:77] op_sel_hi:[1,0]
	v_cvt_pk_bf16_f32 v10, v50, v51
	v_pk_fma_f32 v[54:55], v[8:9], v[62:63], v[84:85]
	v_cvt_pk_bf16_f32 v8, v48, v49
	v_cvt_pk_bf16_f32 v9, v52, v53
	v_cvt_pk_bf16_f32 v11, v54, v55
	ds_read_b128 v[56:59], v138
	ds_read_b128 v[60:63], v140
	global_store_dwordx4 v[172:173], v[8:11], off offset:192
	ds_read_b128 v[82:85], v139
	ds_read_b128 v[86:89], v141
	v_pk_mul_f32 v[40:41], v[40:41], v[76:77] op_sel_hi:[1,0]
	v_pk_mul_f32 v[42:43], v[42:43], v[76:77] op_sel_hi:[1,0]
	v_pk_mul_f32 v[12:13], v[12:13], v[76:77] op_sel_hi:[1,0]
	s_waitcnt lgkmcnt(2)
	v_pk_fma_f32 v[40:41], v[40:41], v[56:57], v[60:61]
	v_pk_fma_f32 v[56:57], v[42:43], v[58:59], v[62:63]
	s_waitcnt lgkmcnt(0)
; #define RT_LOAD(fr, c) do { _Pragma("unroll") for (int i = 0; i < 16; ++i) fr[i] = WFRAG((c) * 16 + i); } while (0)
; template <int MODE>
; __device__ __forceinline__ void norm_phase(const MkArgs& a, LAS unsigned char* lds, const int l, const int wv) {
;     ...
;             u32x4 frA[16], frB[16];
;     ...
;             RT_LOAD(frA, 0); RT_LOAD(frB, 1);
;             RT_MMA(frA, 0);
;             RT_LOAD(frA, 2);
;             RT_MMA(frB, 1);
;             RT_MMA(frA, 2);
	v_pk_fma_f32 v[42:43], v[12:13], v[82:83], v[86:87]
	v_pk_mul_f32 v[12:13], v[14:15], v[76:77] op_sel_hi:[1,0]
	v_cvt_pk_bf16_f32 v14, v42, v43
	v_pk_fma_f32 v[58:59], v[12:13], v[84:85], v[88:89]
	v_cvt_pk_bf16_f32 v12, v40, v41
	v_cvt_pk_bf16_f32 v13, v56, v57
	v_cvt_pk_bf16_f32 v15, v58, v59
	ds_read_b128 v[60:63], v142
	ds_read_b128 v[82:85], v144
	global_store_dwordx4 v[172:173], v[12:15], off offset:256
	ds_read_b128 v[86:89], v143
	ds_read_b128 v[160:163], v145
	v_pk_mul_f32 v[36:37], v[36:37], v[76:77] op_sel_hi:[1,0]
	v_pk_mul_f32 v[38:39], v[38:39], v[76:77] op_sel_hi:[1,0]
	v_pk_mul_f32 v[16:17], v[16:17], v[76:77] op_sel_hi:[1,0]
	s_waitcnt lgkmcnt(2)
	v_pk_fma_f32 v[36:37], v[36:37], v[60:61], v[82:83]
	v_pk_fma_f32 v[60:61], v[38:39], v[62:63], v[84:85]
	s_waitcnt lgkmcnt(0)
	v_pk_fma_f32 v[38:39], v[16:17], v[86:87], v[160:161]
	v_pk_mul_f32 v[16:17], v[18:19], v[76:77] op_sel_hi:[1,0]
	v_cvt_pk_bf16_f32 v18, v38, v39
	v_pk_fma_f32 v[62:63], v[16:17], v[88:89], v[162:163]
	v_cvt_pk_bf16_f32 v16, v36, v37
	v_cvt_pk_bf16_f32 v17, v60, v61
	v_cvt_pk_bf16_f32 v19, v62, v63
	ds_read_b128 v[82:85], v146
	ds_read_b128 v[86:89], v148
	global_store_dwordx4 v[172:173], v[16:19], off offset:320
	ds_read_b128 v[160:163], v147
	ds_read_b128 v[164:167], v149
	v_pk_mul_f32 v[32:33], v[32:33], v[76:77] op_sel_hi:[1,0]
	v_pk_mul_f32 v[34:35], v[34:35], v[76:77] op_sel_hi:[1,0]
	v_pk_mul_f32 v[20:21], v[20:21], v[76:77] op_sel_hi:[1,0]
	s_waitcnt lgkmcnt(2)
	v_pk_fma_f32 v[32:33], v[32:33], v[82:83], v[86:87]
	v_pk_fma_f32 v[82:83], v[34:35], v[84:85], v[88:89]
	s_waitcnt lgkmcnt(0)
	v_pk_fma_f32 v[34:35], v[20:21], v[160:161], v[164:165]
	v_pk_mul_f32 v[20:21], v[22:23], v[76:77] op_sel_hi:[1,0]
	v_cvt_pk_bf16_f32 v22, v34, v35
	v_pk_fma_f32 v[84:85], v[20:21], v[162:163], v[166:167]
	v_cvt_pk_bf16_f32 v20, v32, v33
	v_cvt_pk_bf16_f32 v21, v82, v83
	v_cvt_pk_bf16_f32 v23, v84, v85
	ds_read_b128 v[86:89], v150
	ds_read_b128 v[160:163], v152
	global_store_dwordx4 v[172:173], v[20:23], off offset:384
	ds_read_b128 v[164:167], v151
	ds_read_b128 v[168:171], v153
	v_pk_mul_f32 v[28:29], v[28:29], v[76:77] op_sel_hi:[1,0]
	v_pk_mul_f32 v[30:31], v[30:31], v[76:77] op_sel_hi:[1,0]
	v_pk_mul_f32 v[0:1], v[0:1], v[76:77] op_sel_hi:[1,0]
	s_waitcnt lgkmcnt(2)
	v_pk_fma_f32 v[28:29], v[28:29], v[86:87], v[160:161]
	v_pk_fma_f32 v[86:87], v[30:31], v[88:89], v[162:163]
	s_waitcnt lgkmcnt(0)
	v_pk_fma_f32 v[30:31], v[0:1], v[164:165], v[168:169]
	v_pk_mul_f32 v[0:1], v[2:3], v[76:77] op_sel_hi:[1,0]
	v_cvt_pk_bf16_f32 v2, v30, v31
	v_pk_fma_f32 v[88:89], v[0:1], v[166:167], v[170:171]
	v_cvt_pk_bf16_f32 v0, v28, v29
	v_cvt_pk_bf16_f32 v1, v86, v87
	v_cvt_pk_bf16_f32 v3, v88, v89
	v_mov_b32_e32 v76, v119
	global_store_dwordx4 v[172:173], v[0:3], off offset:448
	global_load_dwordx4 v[160:163], v76, s[22:23]
	global_load_dwordx4 v[164:167], v76, s[22:23] offset:1024
	global_load_dwordx4 v[168:171], v76, s[22:23] offset:2048
	global_load_dwordx4 v[172:175], v76, s[22:23] offset:3072
	s_add_u32 s12, s22, 0x1000
	s_addc_u32 s13, s23, 0
	global_load_dwordx4 v[176:179], v76, s[12:13]
	global_load_dwordx4 v[180:183], v76, s[12:13] offset:1024
	global_load_dwordx4 v[184:187], v76, s[12:13] offset:2048
	global_load_dwordx4 v[188:191], v76, s[12:13] offset:3072
	s_add_u32 s12, s22, 0x2000
	s_addc_u32 s13, s23, 0
	global_load_dwordx4 v[192:195], v76, s[12:13]
	global_load_dwordx4 v[196:199], v76, s[12:13] offset:1024
	global_load_dwordx4 v[200:203], v76, s[12:13] offset:2048
	global_load_dwordx4 v[204:207], v76, s[12:13] offset:3072
	s_add_u32 s12, s22, 0x3000
	s_addc_u32 s13, s23, 0
	global_load_dwordx4 v[208:211], v76, s[12:13]
	global_load_dwordx4 v[212:215], v76, s[12:13] offset:1024
	global_load_dwordx4 v[216:219], v76, s[12:13] offset:2048
	global_load_dwordx4 v[220:223], v76, s[12:13] offset:3072
	s_add_u32 s12, s22, 0x4000
	s_addc_u32 s13, s23, 0
	global_load_dwordx4 v[224:227], v76, s[12:13]
	global_load_dwordx4 v[228:231], v76, s[12:13] offset:1024
	v_lshlrev_b32_e32 v248, 16, v44
	v_and_b32_e32 v249, 0xffff0000, v44
	v_sub_f32_e32 v108, v108, v248
	v_sub_f32_e32 v109, v109, v249
	v_cvt_pk_bf16_f32 v244, v108, v109
	v_lshlrev_b32_e32 v250, 16, v45
	v_and_b32_e32 v251, 0xffff0000, v45
	v_sub_f32_e32 v112, v112, v250
	v_sub_f32_e32 v113, v113, v251
	v_cvt_pk_bf16_f32 v245, v112, v113
	v_lshlrev_b32_e32 v248, 16, v46
	v_and_b32_e32 v249, 0xffff0000, v46
	v_sub_f32_e32 v106, v106, v248
	v_sub_f32_e32 v107, v107, v249
	v_cvt_pk_bf16_f32 v246, v106, v107
	v_lshlrev_b32_e32 v250, 16, v47
	v_and_b32_e32 v251, 0xffff0000, v47
	v_sub_f32_e32 v110, v110, v250
	v_sub_f32_e32 v111, v111, v251
	v_cvt_pk_bf16_f32 v247, v110, v111
	s_waitcnt vmcnt(12)
	v_mfma_f32_16x16x32_bf16 v[232:235], v[44:47], v[160:163], 0
	v_mfma_f32_16x16x32_bf16 v[236:239], v[44:47], v[168:171], 0
	v_mfma_f32_16x16x32_bf16 v[240:243], v[44:47], v[176:179], 0
	v_mfma_f32_16x16x32_bf16 v[232:235], v[44:47], v[164:167], v[232:235]
	v_mfma_f32_16x16x32_bf16 v[236:239], v[44:47], v[172:175], v[236:239]
	v_mfma_f32_16x16x32_bf16 v[240:243], v[44:47], v[180:183], v[240:243]
	v_mfma_f32_16x16x32_bf16 v[232:235], v[244:247], v[160:163], v[232:235]
	v_mfma_f32_16x16x32_bf16 v[236:239], v[244:247], v[168:171], v[236:239]
	v_mfma_f32_16x16x32_bf16 v[240:243], v[244:247], v[176:179], v[240:243]
	global_load_dwordx4 v[160:163], v76, s[12:13] offset:2048
	global_load_dwordx4 v[164:167], v76, s[12:13] offset:3072
	s_add_u32 s12, s22, 0x5000
	s_addc_u32 s13, s23, 0
	global_load_dwordx4 v[168:171], v76, s[12:13]
	global_load_dwordx4 v[172:175], v76, s[12:13] offset:1024
	global_load_dwordx4 v[176:179], v76, s[12:13] offset:2048
	global_load_dwordx4 v[180:183], v76, s[12:13] offset:3072
	v_lshlrev_b32_e32 v248, 16, v24
	v_and_b32_e32 v249, 0xffff0000, v24
	v_sub_f32_e32 v98, v98, v248
	v_sub_f32_e32 v99, v99, v249
	v_cvt_pk_bf16_f32 v244, v98, v99
	v_lshlrev_b32_e32 v250, 16, v25
	v_and_b32_e32 v251, 0xffff0000, v25
	v_sub_f32_e32 v102, v102, v250
	v_sub_f32_e32 v103, v103, v251
	v_cvt_pk_bf16_f32 v245, v102, v103
	v_lshlrev_b32_e32 v248, 16, v26
	v_and_b32_e32 v249, 0xffff0000, v26
	v_sub_f32_e32 v100, v100, v248
	v_sub_f32_e32 v101, v101, v249
	v_cvt_pk_bf16_f32 v246, v100, v101
	v_lshlrev_b32_e32 v250, 16, v27
	v_and_b32_e32 v251, 0xffff0000, v27
	v_sub_f32_e32 v104, v104, v250
	v_sub_f32_e32 v105, v105, v251
	v_cvt_pk_bf16_f32 v247, v104, v105
	s_waitcnt vmcnt(12)
; #define RT_LOAD(fr, c) do { _Pragma("unroll") for (int i = 0; i < 16; ++i) fr[i] = WFRAG((c) * 16 + i); } while (0)
; template <int MODE>
; __device__ __forceinline__ void norm_phase(const MkArgs& a, LAS unsigned char* lds, const int l, const int wv) {
;     ...
;             RT_LOAD(frA, 0); RT_LOAD(frB, 1);
;             RT_MMA(frA, 0);
;             RT_LOAD(frA, 2);
;             RT_MMA(frB, 1);
;             RT_MMA(frA, 2);
	v_mfma_f32_16x16x32_bf16 v[232:235], v[24:27], v[184:187], v[232:235]
	v_mfma_f32_16x16x32_bf16 v[236:239], v[24:27], v[192:195], v[236:239]
	v_mfma_f32_16x16x32_bf16 v[240:243], v[24:27], v[200:203], v[240:243]
	v_mfma_f32_16x16x32_bf16 v[232:235], v[24:27], v[188:191], v[232:235]
	v_mfma_f32_16x16x32_bf16 v[236:239], v[24:27], v[196:199], v[236:239]
	v_mfma_f32_16x16x32_bf16 v[240:243], v[24:27], v[204:207], v[240:243]
	v_mfma_f32_16x16x32_bf16 v[232:235], v[244:247], v[184:187], v[232:235]
	v_mfma_f32_16x16x32_bf16 v[236:239], v[244:247], v[192:195], v[236:239]
	v_mfma_f32_16x16x32_bf16 v[240:243], v[244:247], v[200:203], v[240:243]
	s_add_u32 s12, s22, 0x6000
	s_addc_u32 s13, s23, 0
	global_load_dwordx4 v[184:187], v76, s[12:13]
	global_load_dwordx4 v[188:191], v76, s[12:13] offset:1024
	global_load_dwordx4 v[192:195], v76, s[12:13] offset:2048
	global_load_dwordx4 v[196:199], v76, s[12:13] offset:3072
	s_add_u32 s12, s22, 0x7000
	s_addc_u32 s13, s23, 0
	global_load_dwordx4 v[200:203], v76, s[12:13]
	global_load_dwordx4 v[204:207], v76, s[12:13] offset:1024
	v_lshlrev_b32_e32 v248, 16, v4
	v_and_b32_e32 v249, 0xffff0000, v4
	v_sub_f32_e32 v90, v90, v248
	v_sub_f32_e32 v91, v91, v249
	v_cvt_pk_bf16_f32 v244, v90, v91
	v_lshlrev_b32_e32 v250, 16, v5
	v_and_b32_e32 v251, 0xffff0000, v5
	v_sub_f32_e32 v94, v94, v250
	v_sub_f32_e32 v95, v95, v251
	v_cvt_pk_bf16_f32 v245, v94, v95
	v_lshlrev_b32_e32 v248, 16, v6
	v_and_b32_e32 v249, 0xffff0000, v6
	v_sub_f32_e32 v92, v92, v248
	v_sub_f32_e32 v93, v93, v249
	v_cvt_pk_bf16_f32 v246, v92, v93
	v_lshlrev_b32_e32 v250, 16, v7
	v_and_b32_e32 v251, 0xffff0000, v7
	v_sub_f32_e32 v96, v96, v250
	v_sub_f32_e32 v97, v97, v251
	v_cvt_pk_bf16_f32 v247, v96, v97
	s_waitcnt vmcnt(12)
	v_mfma_f32_16x16x32_bf16 v[232:235], v[4:7], v[208:211], v[232:235]
	v_mfma_f32_16x16x32_bf16 v[236:239], v[4:7], v[216:219], v[236:239]
	v_mfma_f32_16x16x32_bf16 v[240:243], v[4:7], v[224:227], v[240:243]
	v_mfma_f32_16x16x32_bf16 v[232:235], v[4:7], v[212:215], v[232:235]
	v_mfma_f32_16x16x32_bf16 v[236:239], v[4:7], v[220:223], v[236:239]
	v_mfma_f32_16x16x32_bf16 v[240:243], v[4:7], v[228:231], v[240:243]
	v_mfma_f32_16x16x32_bf16 v[232:235], v[244:247], v[208:211], v[232:235]
	v_mfma_f32_16x16x32_bf16 v[236:239], v[244:247], v[216:219], v[236:239]
	v_mfma_f32_16x16x32_bf16 v[240:243], v[244:247], v[224:227], v[240:243]
	global_load_dwordx4 v[208:211], v76, s[12:13] offset:2048
	global_load_dwordx4 v[212:215], v76, s[12:13] offset:3072
	s_add_u32 s12, s22, 0x8000
	s_addc_u32 s13, s23, 0
	global_load_dwordx4 v[216:219], v76, s[12:13]
	global_load_dwordx4 v[220:223], v76, s[12:13] offset:1024
	global_load_dwordx4 v[224:227], v76, s[12:13] offset:2048
	global_load_dwordx4 v[228:231], v76, s[12:13] offset:3072
	v_lshlrev_b32_e32 v248, 16, v8
	v_and_b32_e32 v249, 0xffff0000, v8
	v_sub_f32_e32 v48, v48, v248
	v_sub_f32_e32 v49, v49, v249
	v_cvt_pk_bf16_f32 v244, v48, v49
	v_lshlrev_b32_e32 v250, 16, v9
	v_and_b32_e32 v251, 0xffff0000, v9
	v_sub_f32_e32 v52, v52, v250
	v_sub_f32_e32 v53, v53, v251
	v_cvt_pk_bf16_f32 v245, v52, v53
	v_lshlrev_b32_e32 v248, 16, v10
	v_and_b32_e32 v249, 0xffff0000, v10
	v_sub_f32_e32 v50, v50, v248
	v_sub_f32_e32 v51, v51, v249
	v_cvt_pk_bf16_f32 v246, v50, v51
	v_lshlrev_b32_e32 v250, 16, v11
	v_and_b32_e32 v251, 0xffff0000, v11
	v_sub_f32_e32 v54, v54, v250
	v_sub_f32_e32 v55, v55, v251
	v_cvt_pk_bf16_f32 v247, v54, v55
	s_waitcnt vmcnt(12)
	v_mfma_f32_16x16x32_bf16 v[232:235], v[8:11], v[160:163], v[232:235]
	v_mfma_f32_16x16x32_bf16 v[236:239], v[8:11], v[168:171], v[236:239]
	v_mfma_f32_16x16x32_bf16 v[240:243], v[8:11], v[176:179], v[240:243]
	v_mfma_f32_16x16x32_bf16 v[232:235], v[8:11], v[164:167], v[232:235]
	v_mfma_f32_16x16x32_bf16 v[236:239], v[8:11], v[172:175], v[236:239]
	v_mfma_f32_16x16x32_bf16 v[240:243], v[8:11], v[180:183], v[240:243]
	v_mfma_f32_16x16x32_bf16 v[232:235], v[244:247], v[160:163], v[232:235]
	v_mfma_f32_16x16x32_bf16 v[236:239], v[244:247], v[168:171], v[236:239]
	v_mfma_f32_16x16x32_bf16 v[240:243], v[244:247], v[176:179], v[240:243]
	s_add_u32 s12, s22, 0x9000
	s_addc_u32 s13, s23, 0
	global_load_dwordx4 v[160:163], v76, s[12:13]
	global_load_dwordx4 v[164:167], v76, s[12:13] offset:1024
	global_load_dwordx4 v[168:171], v76, s[12:13] offset:2048
	global_load_dwordx4 v[172:175], v76, s[12:13] offset:3072
	s_add_u32 s12, s22, 0xa000
	s_addc_u32 s13, s23, 0
	global_load_dwordx4 v[176:179], v76, s[12:13]
	global_load_dwordx4 v[180:183], v76, s[12:13] offset:1024
	v_lshlrev_b32_e32 v248, 16, v12
	v_and_b32_e32 v249, 0xffff0000, v12
	v_sub_f32_e32 v40, v40, v248
	v_sub_f32_e32 v41, v41, v249
	v_cvt_pk_bf16_f32 v244, v40, v41
	v_lshlrev_b32_e32 v250, 16, v13
	v_and_b32_e32 v251, 0xffff0000, v13
	v_sub_f32_e32 v56, v56, v250
	v_sub_f32_e32 v57, v57, v251
	v_cvt_pk_bf16_f32 v245, v56, v57
	v_lshlrev_b32_e32 v248, 16, v14
	v_and_b32_e32 v249, 0xffff0000, v14
	v_sub_f32_e32 v42, v42, v248
	v_sub_f32_e32 v43, v43, v249
	v_cvt_pk_bf16_f32 v246, v42, v43
	v_lshlrev_b32_e32 v250, 16, v15
	v_and_b32_e32 v251, 0xffff0000, v15
	v_sub_f32_e32 v58, v58, v250
	v_sub_f32_e32 v59, v59, v251
	v_cvt_pk_bf16_f32 v247, v58, v59
	s_waitcnt vmcnt(12)
; #define RT_LOAD(fr, c) do { _Pragma("unroll") for (int i = 0; i < 16; ++i) fr[i] = WFRAG((c) * 16 + i); } while (0)
; template <int MODE>
; __device__ __forceinline__ void norm_phase(const MkArgs& a, LAS unsigned char* lds, const int l, const int wv) {
;     ...
;             RT_LOAD(frA, 0); RT_LOAD(frB, 1);
;             RT_MMA(frA, 0);
;             RT_LOAD(frA, 2);
;             RT_MMA(frB, 1);
;             RT_MMA(frA, 2);
;     ...
; #pragma unroll
;             for (int nt = 0; nt < 3; ++nt)
; #pragma unroll
;                 for (int e = 0; e < 4; ++e) part[(w * 16 + 4 * q + e) * 48 + 16 * nt + r] = acc[nt][e];
;     ...
;             __syncthreads();
;             for (int o = tid; o < 16 * 36; o += 512) {
	v_mfma_f32_16x16x32_bf16 v[232:235], v[12:15], v[184:187], v[232:235]
	v_mfma_f32_16x16x32_bf16 v[236:239], v[12:15], v[192:195], v[236:239]
	v_mfma_f32_16x16x32_bf16 v[240:243], v[12:15], v[200:203], v[240:243]
	v_mfma_f32_16x16x32_bf16 v[232:235], v[12:15], v[188:191], v[232:235]
	v_mfma_f32_16x16x32_bf16 v[236:239], v[12:15], v[196:199], v[236:239]
	v_mfma_f32_16x16x32_bf16 v[240:243], v[12:15], v[204:207], v[240:243]
	v_mfma_f32_16x16x32_bf16 v[232:235], v[244:247], v[184:187], v[232:235]
	v_mfma_f32_16x16x32_bf16 v[236:239], v[244:247], v[192:195], v[236:239]
	v_mfma_f32_16x16x32_bf16 v[240:243], v[244:247], v[200:203], v[240:243]
	global_load_dwordx4 v[184:187], v76, s[12:13] offset:2048
	global_load_dwordx4 v[188:191], v76, s[12:13] offset:3072
	s_add_u32 s12, s22, 0xb000
	s_addc_u32 s13, s23, 0
	global_load_dwordx4 v[192:195], v76, s[12:13]
	global_load_dwordx4 v[196:199], v76, s[12:13] offset:1024
	global_load_dwordx4 v[200:203], v76, s[12:13] offset:2048
	global_load_dwordx4 v[204:207], v76, s[12:13] offset:3072
	v_lshlrev_b32_e32 v248, 16, v16
	v_and_b32_e32 v249, 0xffff0000, v16
	v_sub_f32_e32 v36, v36, v248
	v_sub_f32_e32 v37, v37, v249
	v_cvt_pk_bf16_f32 v244, v36, v37
	v_lshlrev_b32_e32 v250, 16, v17
	v_and_b32_e32 v251, 0xffff0000, v17
	v_sub_f32_e32 v60, v60, v250
	v_sub_f32_e32 v61, v61, v251
	v_cvt_pk_bf16_f32 v245, v60, v61
	v_lshlrev_b32_e32 v248, 16, v18
	v_and_b32_e32 v249, 0xffff0000, v18
	v_sub_f32_e32 v38, v38, v248
	v_sub_f32_e32 v39, v39, v249
	v_cvt_pk_bf16_f32 v246, v38, v39
	v_lshlrev_b32_e32 v250, 16, v19
	v_and_b32_e32 v251, 0xffff0000, v19
	v_sub_f32_e32 v62, v62, v250
	v_sub_f32_e32 v63, v63, v251
	v_cvt_pk_bf16_f32 v247, v62, v63
	s_waitcnt vmcnt(12)
	v_mfma_f32_16x16x32_bf16 v[232:235], v[16:19], v[208:211], v[232:235]
	v_mfma_f32_16x16x32_bf16 v[236:239], v[16:19], v[216:219], v[236:239]
	v_mfma_f32_16x16x32_bf16 v[240:243], v[16:19], v[224:227], v[240:243]
	v_mfma_f32_16x16x32_bf16 v[232:235], v[16:19], v[212:215], v[232:235]
	v_mfma_f32_16x16x32_bf16 v[236:239], v[16:19], v[220:223], v[236:239]
	v_mfma_f32_16x16x32_bf16 v[240:243], v[16:19], v[228:231], v[240:243]
	v_mfma_f32_16x16x32_bf16 v[232:235], v[244:247], v[208:211], v[232:235]
	v_mfma_f32_16x16x32_bf16 v[236:239], v[244:247], v[216:219], v[236:239]
	v_mfma_f32_16x16x32_bf16 v[240:243], v[244:247], v[224:227], v[240:243]
	v_lshlrev_b32_e32 v248, 16, v20
	v_and_b32_e32 v249, 0xffff0000, v20
	v_sub_f32_e32 v32, v32, v248
	v_sub_f32_e32 v33, v33, v249
	v_cvt_pk_bf16_f32 v244, v32, v33
	v_lshlrev_b32_e32 v250, 16, v21
	v_and_b32_e32 v251, 0xffff0000, v21
	v_sub_f32_e32 v82, v82, v250
	v_sub_f32_e32 v83, v83, v251
	v_cvt_pk_bf16_f32 v245, v82, v83
	v_lshlrev_b32_e32 v248, 16, v22
	v_and_b32_e32 v249, 0xffff0000, v22
	v_sub_f32_e32 v34, v34, v248
	v_sub_f32_e32 v35, v35, v249
	v_cvt_pk_bf16_f32 v246, v34, v35
	v_lshlrev_b32_e32 v250, 16, v23
	v_and_b32_e32 v251, 0xffff0000, v23
	v_sub_f32_e32 v84, v84, v250
	v_sub_f32_e32 v85, v85, v251
	v_cvt_pk_bf16_f32 v247, v84, v85
	s_waitcnt vmcnt(6)
	v_mfma_f32_16x16x32_bf16 v[232:235], v[20:23], v[160:163], v[232:235]
	v_mfma_f32_16x16x32_bf16 v[236:239], v[20:23], v[168:171], v[236:239]
	v_mfma_f32_16x16x32_bf16 v[240:243], v[20:23], v[176:179], v[240:243]
	v_mfma_f32_16x16x32_bf16 v[232:235], v[20:23], v[164:167], v[232:235]
	v_mfma_f32_16x16x32_bf16 v[236:239], v[20:23], v[172:175], v[236:239]
	v_mfma_f32_16x16x32_bf16 v[240:243], v[20:23], v[180:183], v[240:243]
	v_mfma_f32_16x16x32_bf16 v[232:235], v[244:247], v[160:163], v[232:235]
	v_mfma_f32_16x16x32_bf16 v[236:239], v[244:247], v[168:171], v[236:239]
	v_mfma_f32_16x16x32_bf16 v[240:243], v[244:247], v[176:179], v[240:243]
	v_lshlrev_b32_e32 v248, 16, v0
	v_and_b32_e32 v249, 0xffff0000, v0
	v_sub_f32_e32 v28, v28, v248
	v_sub_f32_e32 v29, v29, v249
	v_cvt_pk_bf16_f32 v244, v28, v29
	v_lshlrev_b32_e32 v250, 16, v1
	v_and_b32_e32 v251, 0xffff0000, v1
	v_sub_f32_e32 v86, v86, v250
	v_sub_f32_e32 v87, v87, v251
	v_cvt_pk_bf16_f32 v245, v86, v87
	v_lshlrev_b32_e32 v248, 16, v2
	v_and_b32_e32 v249, 0xffff0000, v2
	v_sub_f32_e32 v30, v30, v248
	v_sub_f32_e32 v31, v31, v249
	v_cvt_pk_bf16_f32 v246, v30, v31
	v_lshlrev_b32_e32 v250, 16, v3
	v_and_b32_e32 v251, 0xffff0000, v3
	v_sub_f32_e32 v88, v88, v250
	v_sub_f32_e32 v89, v89, v251
	v_cvt_pk_bf16_f32 v247, v88, v89
	s_waitcnt vmcnt(0)
	v_mfma_f32_16x16x32_bf16 v[232:235], v[0:3], v[184:187], v[232:235]
	v_mfma_f32_16x16x32_bf16 v[236:239], v[0:3], v[192:195], v[236:239]
	v_mfma_f32_16x16x32_bf16 v[240:243], v[0:3], v[200:203], v[240:243]
	v_mfma_f32_16x16x32_bf16 v[232:235], v[0:3], v[188:191], v[232:235]
	v_mfma_f32_16x16x32_bf16 v[236:239], v[0:3], v[196:199], v[236:239]
	v_mfma_f32_16x16x32_bf16 v[240:243], v[0:3], v[204:207], v[240:243]
	v_mfma_f32_16x16x32_bf16 v[232:235], v[244:247], v[184:187], v[232:235]
	v_mfma_f32_16x16x32_bf16 v[236:239], v[244:247], v[192:195], v[236:239]
	v_mfma_f32_16x16x32_bf16 v[240:243], v[244:247], v[200:203], v[240:243]
	v_add_u32_e32 v4, 0x400, v156
	s_nop 7
	s_nop 1
	ds_write2_b32 v4, v232, v236 offset1:16
	ds_write2_b32 v4, v234, v238 offset0:96 offset1:112
	ds_write2_b32 v4, v240, v233 offset0:32 offset1:48
	ds_write2_b32 v4, v237, v241 offset0:64 offset1:80
	ds_write2_b32 v4, v242, v235 offset0:128 offset1:144
	ds_write2_b32 v4, v239, v243 offset0:160 offset1:176
	s_waitcnt lgkmcnt(0)
	s_barrier
	s_and_saveexec_b64 s[12:13], s[6:7]
	s_cbranch_execz .LBB0_1976
	s_mov_b64 s[14:15], 0
	v_mov_b32_e32 v0, v114
	v_mov_b32_e32 v2, v64
